# gate/up GEMM: dropped the post-epilogue vmcnt(0) that only drained the unit's 8 output stores (loads it guarded are waited for before the epilogue); stores now drain under the next unit's K loop
# speedup vs baseline: 1.0008x; 1.0008x over previous
.LBB0_718:
	s_nop 0
	s_waitcnt lgkmcnt(0)
	s_andn2_b64 vcc, exec, s[42:43]
	s_cbranch_vccnz .LBB0_721
	s_andn2_b64 vcc, exec, s[44:45]
	s_cbranch_vccnz .LBB0_685
	s_barrier
	s_branch .LBB0_685

.LBB0_1794:
	s_nop 0
	s_waitcnt lgkmcnt(0)
	s_andn2_b64 vcc, exec, s[38:39]
	s_cbranch_vccnz .LBB0_1797
	s_andn2_b64 vcc, exec, s[40:41]
	s_cbranch_vccnz .LBB0_1761
	s_barrier
	s_branch .LBB0_1761
